# phase D: unit index ranges 320..351 and 1056..1087 trade places so the extra fifth units are spread evenly over cheap and expensive halves
# speedup vs baseline: 1.0172x; 1.0055x over previous
.LBB0_631:
	s_sub_u32 s100, s18, 0x140
	s_cmp_lt_u32 s100, 32
	s_cselect_b32 s101, 0x2e0, 0
	s_sub_u32 s100, s18, 0x420
	s_cmp_lt_u32 s100, 32
	s_cselect_b32 s100, 0xfffffd20, 0
	s_add_i32 s100, s100, s101
	s_add_i32 s100, s100, s18
	s_mul_hi_i32 s6, s100, 0x78787879
	s_lshr_b32 s7, s6, 31
	s_ashr_i32 s36, s6, 8
	s_add_i32 s36, s36, s7
	s_mul_i32 s6, s36, 0x220
	s_sub_i32 s42, s100, s6
	s_ashr_i32 s68, s42, 2
	s_lshl_b32 s50, s68, 6
	s_add_i32 s6, s50, 0x7fffe000
	s_and_b32 s6, s6, 0x7fffff00
	s_add_i32 s28, s6, 0x2000
	s_and_b32 s51, s50, 0xfffff000
	s_cmpk_lt_i32 s68, 0x80
	s_cselect_b64 s[6:7], -1, 0
	s_and_b64 s[40:41], s[6:7], exec
	s_cselect_b32 s40, s75, 0xc0
	s_cselect_b32 s28, s51, s28
	s_lshl_b32 s41, s42, 4
	s_and_b32 s40, s40, s50
	s_and_b32 s41, s41, 48
	s_or_b32 s40, s40, s41
	s_mov_b32 s42, 0x1100000
	s_cmpk_lt_i32 s100, 0x220
	s_cbranch_scc1 .LBB0_637
	s_and_saveexec_b64 s[58:59], s[2:3]
	s_cbranch_execz .LBB0_634
	s_and_b64 s[6:7], s[6:7], exec
	v_add_u32_e32 v14, s40, v73
	s_movk_i32 s6, 0x1000
	v_add_u32_e32 v2, s28, v14
	v_mov_b64_e32 v[0:1], s[10:11]
	s_cselect_b32 s41, s6, 0x100
	v_mad_i64_i32 v[0:1], s[6:7], v2, s95, v[0:1]
	v_lshl_add_u64 v[8:9], v[28:29], 1, v[0:1]
	s_mov_b64 s[6:7], 0x1000
	v_lshl_add_u64 v[12:13], v[8:9], 0, s[6:7]
	v_add_co_u32_e32 v8, vcc, 0x1000, v8
	global_load_dwordx4 v[0:3], v[30:31], off offset:16
	global_load_dwordx4 v[16:19], v[30:31], off
	global_load_dwordx4 v[4:7], v[32:33], off offset:16
	global_load_dwordx4 v[20:23], v[32:33], off
	v_addc_co_u32_e32 v9, vcc, 0, v9, vcc
	global_load_dwordx4 v[8:11], v[8:9], off
	v_add_u32_e32 v15, 1, v14
	v_cmp_gt_i32_e32 vcc, s41, v15
	v_cmp_lt_i32_e64 s[6:7], 0, v14
	s_waitcnt vmcnt(3)
	v_mov_b32_e32 v50, v16
	v_cndmask_b32_e32 v104, 0, v186, vcc
	s_waitcnt vmcnt(1)
	v_mov_b32_e32 v51, v20
	v_mov_b32_e32 v20, v17
	s_waitcnt vmcnt(0)
	v_lshlrev_b32_e32 v42, 16, v8
	v_and_b32_e32 v44, 0xffff0000, v8
	v_lshlrev_b32_e32 v46, 16, v9
	v_and_b32_e32 v40, 0xffff0000, v9
	v_cndmask_b32_e64 v9, 0, -1, s[6:7]
	v_cndmask_b32_e64 v8, 0, v185, s[6:7]
	v_lshl_add_u64 v[8:9], v[12:13], 0, v[8:9]
	v_lshl_add_u64 v[12:13], v[12:13], 0, v[104:105]
	v_lshlrev_b32_e32 v38, 16, v10
	v_and_b32_e32 v36, 0xffff0000, v10
	v_lshlrev_b32_e32 v26, 16, v11
	v_and_b32_e32 v24, 0xffff0000, v11
	global_load_dwordx4 v[8:11], v[8:9], off
	s_nop 0
	global_load_dwordx4 v[12:15], v[12:13], off
	s_waitcnt vmcnt(1)
	v_lshlrev_b32_e32 v39, 16, v8
	v_cndmask_b32_e64 v48, 0, v39, s[6:7]
	s_waitcnt vmcnt(0)
	v_lshlrev_b32_e32 v41, 16, v12
	v_cndmask_b32_e32 v49, 0, v41, vcc
	v_pk_add_f32 v[48:49], v[48:49], v[42:43] op_sel_hi:[1,0] neg_lo:[0,1] neg_hi:[0,1]
	v_and_b32_e32 v12, 0xffff0000, v12
	v_pk_mul_f32 v[48:49], v[50:51], v[48:49]
	v_and_b32_e32 v8, 0xffff0000, v8
	v_add_f32_e32 v16, v48, v42
	v_cndmask_b32_e32 v43, 0, v12, vcc
	v_cndmask_b32_e64 v42, 0, v8, s[6:7]
	v_pk_add_f32 v[42:43], v[42:43], v[44:45] op_sel_hi:[1,0] neg_lo:[0,1] neg_hi:[0,1]
	v_lshlrev_b32_e32 v17, 16, v13
	v_pk_mul_f32 v[20:21], v[20:21], v[42:43]
	v_mov_b32_e32 v42, v18
	v_add_f32_e32 v8, v20, v44
	v_add_f32_e32 v8, v8, v21
	v_mul_f32_e32 v8, 0xbfb8aa3b, v8
	v_exp_f32_e32 v8, v8
	v_cndmask_b32_e32 v21, 0, v17, vcc
	v_mov_b32_e32 v43, v22
	v_mov_b32_e32 v22, v19
	v_add_f32_e32 v8, 1.0, v8
	v_rcp_f32_e32 v12, v8
	v_lshlrev_b32_e32 v8, 16, v9
	v_cndmask_b32_e64 v20, 0, v8, s[6:7]
	v_pk_add_f32 v[20:21], v[20:21], v[46:47] op_sel_hi:[1,0] neg_lo:[0,1] neg_hi:[0,1]
	v_mov_b32_e32 v18, v0
	v_pk_mul_f32 v[20:21], v[42:43], v[20:21]
	v_mov_b32_e32 v19, v4
	v_add_f32_e32 v8, v20, v46
	v_add_f32_e32 v8, v8, v21
	v_mul_f32_e32 v8, 0xbfb8aa3b, v8
	v_exp_f32_e32 v8, v8
	v_and_b32_e32 v4, 0xffff0000, v10
	v_and_b32_e32 v27, 0xffff0000, v11
	v_and_b32_e32 v25, 0xffff0000, v15
	v_add_f32_e32 v8, 1.0, v8
	v_rcp_f32_e32 v17, v8
	v_and_b32_e32 v8, 0xffff0000, v13
	v_and_b32_e32 v13, 0xffff0000, v9
	v_cndmask_b32_e32 v9, 0, v8, vcc
	v_cndmask_b32_e64 v8, 0, v13, s[6:7]
	v_pk_add_f32 v[8:9], v[8:9], v[40:41] op_sel_hi:[1,0] neg_lo:[0,1] neg_hi:[0,1]
	v_add_f32_e32 v16, v16, v49
	v_pk_mul_f32 v[8:9], v[22:23], v[8:9]
	v_mul_f32_e32 v16, 0xbfb8aa3b, v16
	v_add_f32_e32 v8, v8, v40
	v_add_f32_e32 v8, v8, v9
	v_mul_f32_e32 v8, 0xbfb8aa3b, v8
	v_exp_f32_e32 v8, v8
	v_lshlrev_b32_e32 v9, 16, v14
	v_cndmask_b32_e32 v9, 0, v9, vcc
	v_exp_f32_e32 v16, v16
	v_add_f32_e32 v8, 1.0, v8
	v_rcp_f32_e32 v13, v8
	v_lshlrev_b32_e32 v8, 16, v10
	v_cndmask_b32_e64 v8, 0, v8, s[6:7]
	v_pk_add_f32 v[8:9], v[8:9], v[38:39] op_sel_hi:[1,0] neg_lo:[0,1] neg_hi:[0,1]
	v_add_f32_e32 v16, 1.0, v16
	v_pk_mul_f32 v[8:9], v[18:19], v[8:9]
	v_rcp_f32_e32 v16, v16
	v_add_f32_e32 v0, v8, v38
	v_add_f32_e32 v0, v0, v9
	v_mul_f32_e32 v0, 0xbfb8aa3b, v0
	v_exp_f32_e32 v0, v0
	v_cndmask_b32_e64 v8, 0, v4, s[6:7]
	v_mov_b32_e32 v4, v1
	v_add_f32_e32 v0, 1.0, v0
	v_rcp_f32_e32 v18, v0
	v_and_b32_e32 v0, 0xffff0000, v14
	v_cndmask_b32_e32 v9, 0, v0, vcc
	v_pk_add_f32 v[8:9], v[8:9], v[36:37] op_sel_hi:[1,0] neg_lo:[0,1] neg_hi:[0,1]
	s_nop 0
	v_pk_mul_f32 v[0:1], v[4:5], v[8:9]
	v_mov_b32_e32 v4, v2
	v_add_f32_e32 v0, v0, v36
	v_add_f32_e32 v0, v0, v1
	v_mul_f32_e32 v0, 0xbfb8aa3b, v0
	v_exp_f32_e32 v0, v0
	v_lshlrev_b32_e32 v1, 16, v15
	v_cndmask_b32_e32 v1, 0, v1, vcc
	v_mov_b32_e32 v5, v6
	v_add_f32_e32 v0, 1.0, v0
	v_rcp_f32_e32 v8, v0
	v_lshlrev_b32_e32 v0, 16, v11
	v_cndmask_b32_e64 v0, 0, v0, s[6:7]
	v_pk_add_f32 v[0:1], v[0:1], v[26:27] op_sel_hi:[1,0] neg_lo:[0,1] neg_hi:[0,1]
	v_mov_b32_e32 v6, v3
	v_pk_mul_f32 v[0:1], v[4:5], v[0:1]
	v_cvt_pk_bf16_f32 v2, v18, v8
	v_add_f32_e32 v0, v0, v26
	v_add_f32_e32 v0, v0, v1
	v_mul_f32_e32 v0, 0xbfb8aa3b, v0
	v_exp_f32_e32 v0, v0
	v_cndmask_b32_e32 v1, 0, v25, vcc
	v_add_f32_e32 v0, 1.0, v0
	v_rcp_f32_e32 v4, v0
	v_cndmask_b32_e64 v0, 0, v27, s[6:7]
	v_pk_add_f32 v[0:1], v[0:1], v[24:25] op_sel_hi:[1,0] neg_lo:[0,1] neg_hi:[0,1]
	s_nop 0
	v_pk_mul_f32 v[0:1], v[6:7], v[0:1]
	s_nop 0
	v_add_f32_e32 v0, v0, v24
	v_add_f32_e32 v0, v0, v1
	v_mul_f32_e32 v0, 0xbfb8aa3b, v0
	v_exp_f32_e32 v0, v0
	v_cvt_pk_bf16_f32 v1, v17, v13
	v_add_f32_e32 v0, 1.0, v0
	v_rcp_f32_e32 v3, v0
	v_cvt_pk_bf16_f32 v0, v16, v12
	v_cvt_pk_bf16_f32 v3, v4, v3
	ds_write_b128 v74, v[0:3]
